# nt11 + Infinity-Cache pre-warm: touch loads over the int8 u table at the start of phase 8
# baseline (speedup 1.0000x reference)
; #define LAS __attribute__((address_space(3)))
; __device__ __forceinline__ void p8_topk(Frame& F) {
;     constexpr CandTab CT = make_cand();
;     const float* ST = (const float*)(F.ws + WS_ST); int* EXP = (int*)(F.ws + WS_EXP); float* GATE = (float*)(F.ws + WS_GATE);
;     int* ES = (int*)(F.ws + WS_ES); float* GS = (float*)(F.ws + WS_GS); int* BST = (int*)(F.ws + WS_BST);
;     LAS int* EL = (LAS int*)(F.lds + RING_OFF); LAS float* GL = (LAS float*)(F.lds + RING_OFF + 16384);
;     LAS int* tab = (LAS int*)(F.lds + RING_OFF + 32768 + F.wave * 8192);
;     const int lane = F.lane, tl = lane & 31, c = lane >> 5, h = F.wave;
;     for (int u = F.vcu; u < T_ / 32; u += F.G) {
;         const int t = u * 32 + tl;
;         int mine[16];
;         topk128(ST + (size_t)((h * 2 + c) * 128) * T_ + t, mine);
;         float s1[16], s2[16];
; #pragma unroll
;         for (int i = 0; i < 16; ++i) { const int other = __shfl_xor(mine[i], 32); const int k1 = c ? other : mine[i], k2 = c ? mine[i] : other;
;             s1[i] = kval(k1 & ~0x7F); s2[i] = kval(k2 & ~0x7F); tab[i * 64 + lane] = k1 & 0x7F; tab[(16 + i) * 64 + lane] = k2 & 0x7F; }
;         int c0[16], c1[16], c2[16], c3[16];
; #pragma unroll
;         for (int i = 0; i < 16; ++i) {
;             c0[i] = CT.a[i] < 0 ? (int)0x80000000 : ((fkey(s1[CT.a[i] < 0 ? 0 : CT.a[i]] + s2[CT.b[i] < 0 ? 0 : CT.b[i]]) & ~0xFF) | (CT.a[i] * 16 + CT.b[i]));
;             c1[i] = CT.a[16 + i] < 0 ? (int)0x80000000 : ((fkey(s1[CT.a[16 + i] < 0 ? 0 : CT.a[16 + i]] + s2[CT.b[16 + i] < 0 ? 0 : CT.b[16 + i]]) & ~0xFF) | (CT.a[16 + i] * 16 + CT.b[16 + i]));
;             c2[i] = CT.a[32 + i] < 0 ? (int)0x80000000 : ((fkey(s1[CT.a[32 + i] < 0 ? 0 : CT.a[32 + i]] + s2[CT.b[32 + i] < 0 ? 0 : CT.b[32 + i]]) & ~0xFF) | (CT.a[32 + i] * 16 + CT.b[32 + i]));
;             c3[i] = CT.a[48 + i] < 0 ? (int)0x80000000 : ((fkey(s1[CT.a[48 + i] < 0 ? 0 : CT.a[48 + i]] + s2[CT.b[48 + i] < 0 ? 0 : CT.b[48 + i]]) & ~0xFF) | (CT.a[48 + i] * 16 + CT.b[48 + i]));
;         }
;         sort16_desc(c0); sort16_desc(c1); sort16_desc(c2); sort16_desc(c3);
;         merge_top16(c0, c1); merge_top16(c2, c3); merge_top16(c0, c2);
;         LDS_WAIT();
;         float rs = 1.0f;
;         if (DEFER_FFN_NORM) { const float* sp_ = (const float*)(F.ws + WS_SSQP) + (size_t)t * 64; float a_ = 0.f;
; #pragma unroll
.LBB0_770:
	v_readlane_b32 s4, v255, 11
	v_readlane_b32 s5, v255, 12
	s_cmp_lt_i32 s4, 9
	s_cselect_b64 s[4:5], -1, 0
	s_and_b64 s[0:1], s[4:5], s[0:1]
	v_writelane_b32 v255, s0, 15
	s_andn2_b64 vcc, exec, s[0:1]
	s_nop 0
	v_writelane_b32 v255, s1, 16
	s_cbranch_vccnz .LBB0_789
	s_cmpk_gt_i32 s97, 0xff
	s_cbranch_scc1 .LBB0_789
	v_writelane_b32 v255, s2, 17
	s_lshl_b32 s98, s97, 18
	s_add_u32 s98, s98, 0x35700000
	s_add_u32 s98, s66, s98
	s_addc_u32 s99, s67, 0
	v_readlane_b32 s100, v255, 10
	s_lshl_b32 s100, s100, 15
	v_lshlrev_b32_e32 v250, 9, v202
	s_nop 1
	v_add_u32_e32 v250, s100, v250
	s_nop 4
	global_load_dword v251, v250, s[98:99]
	global_load_dword v251, v250, s[98:99] offset:64
	global_load_dword v251, v250, s[98:99] offset:128
	global_load_dword v251, v250, s[98:99] offset:192
	global_load_dword v251, v250, s[98:99] offset:256
	global_load_dword v251, v250, s[98:99] offset:320
	global_load_dword v251, v250, s[98:99] offset:384
	global_load_dword v251, v250, s[98:99] offset:448
	s_waitcnt vmcnt(7)
	v_lshlrev_b32_e32 v2, 2, v0
	s_add_u32 s56, s66, 0x13c00000
	v_readlane_b32 s4, v255, 10
	v_and_b32_e32 v2, 0x80, v2
	s_addc_u32 s57, s67, 0
	v_lshl_or_b32 v2, s4, 8, v2
	s_add_u32 s58, s66, 0x14000000
	s_waitcnt lgkmcnt(0)
	v_ashrrev_i32_e32 v3, 31, v2
	s_addc_u32 s59, s67, 0
	s_lshl_b32 s0, s4, 13
	v_lshlrev_b64 v[2:3], 15, v[2:3]
	s_add_i32 s2, s0, 0
	s_waitcnt vmcnt(6)
	v_lshl_add_u64 v[14:15], s[8:9], 0, v[2:3]
	v_mbcnt_lo_u32_b32 v2, -1, 0
	v_mbcnt_hi_u32_b32 v6, -1, v2
	s_cmp_lt_u32 s3, 64
	v_and_b32_e32 v3, 64, v6
	v_cmp_gt_u32_e64 s[52:53], 32, v202
	s_cselect_b64 s[0:1], -1, 0
	v_xor_b32_e32 v2, 32, v6
	v_add_u32_e32 v7, 64, v3
	s_and_b64 s[0:1], s[0:1], s[52:53]
	v_cmp_lt_i32_e32 vcc, v2, v7
	v_writelane_b32 v255, s0, 18
	v_mov_b32_e32 v3, 0
	v_cndmask_b32_e32 v2, v6, v2, vcc
	v_writelane_b32 v255, s1, 19
	s_lshl_b32 s0, s4, 4
	s_lshl_b32 s1, s4, 6
	v_lshlrev_b32_e32 v17, 2, v2
	v_lshlrev_b32_e32 v2, 2, v202
	s_add_u32 s1, s66, s1
	s_waitcnt vmcnt(1)
	v_add_u32_e32 v26, s2, v2
	s_addc_u32 s2, s67, 0
	s_add_u32 s6, s1, 0x34f00000
	s_addc_u32 s7, s2, 0
	v_writelane_b32 v255, s6, 20
	v_lshl_add_u32 v8, v202, 7, s0
	v_lshl_add_u64 v[4:5], s[66:67], 0, v[2:3]
	v_writelane_b32 v255, s7, 21
	s_add_u32 s6, s1, 0x35300000
	s_addc_u32 s7, s2, 0
	v_writelane_b32 v255, s6, 22
	v_cmp_gt_u32_e64 s[0:1], 16, v202
	v_and_b32_e32 v3, 2, v0
	v_writelane_b32 v255, s7, 23
	v_writelane_b32 v255, s0, 24
	v_cmp_ne_u32_e32 vcc, 0, v3
	v_cmp_eq_u32_e64 s[10:11], 0, v3
	v_writelane_b32 v255, s1, 25
	s_mov_b64 s[0:1], 0x14400000
	v_lshl_add_u64 v[18:19], v[4:5], 0, s[0:1]
	v_xor_b32_e32 v4, 1, v6
	v_cmp_lt_i32_e64 s[0:1], v4, v7
	v_xor_b32_e32 v5, 2, v6
	v_and_b32_e32 v3, 8, v0
	v_cndmask_b32_e64 v4, v6, v4, s[0:1]
	v_lshlrev_b32_e32 v28, 2, v4
	v_and_b32_e32 v4, 1, v0
	v_cmp_eq_u32_e64 s[6:7], 0, v4
	s_xor_b64 s[0:1], vcc, s[6:7]
	v_writelane_b32 v255, s0, 26
	v_and_b32_e32 v4, 4, v0
	v_cmp_ne_u32_e32 vcc, 0, v4
	v_writelane_b32 v255, s1, 27
	v_cmp_lt_i32_e64 s[0:1], v5, v7
	s_xor_b64 s[14:15], vcc, s[6:7]
	v_cmp_eq_u32_e64 s[16:17], 0, v4
	v_cndmask_b32_e64 v5, v6, v5, s[0:1]
	s_xor_b64 s[0:1], vcc, s[10:11]
	v_lshlrev_b32_e32 v29, 2, v5
	v_writelane_b32 v255, s0, 28
	v_xor_b32_e32 v5, 4, v6
	v_cmp_ne_u32_e32 vcc, 0, v3
	v_writelane_b32 v255, s1, 29
	v_cmp_lt_i32_e64 s[0:1], v5, v7
	v_and_b32_e32 v4, 16, v0
	s_xor_b64 s[18:19], vcc, s[16:17]
	v_cndmask_b32_e64 v5, v6, v5, s[0:1]
	v_lshlrev_b32_e32 v30, 2, v5
	v_xor_b32_e32 v5, 8, v6
	v_cmp_lt_i32_e64 s[0:1], v5, v7
	s_xor_b64 s[20:21], vcc, s[10:11]
	s_xor_b64 s[22:23], vcc, s[6:7]
	v_cndmask_b32_e64 v5, v6, v5, s[0:1]
	v_lshlrev_b32_e32 v31, 2, v5
	v_xor_b32_e32 v5, 16, v6
	v_cmp_lt_i32_e64 s[0:1], v5, v7
	v_cmp_ne_u32_e32 vcc, 0, v4
	v_cmp_eq_u32_e64 s[24:25], 0, v3
	v_cndmask_b32_e64 v5, v6, v5, s[0:1]
	v_cmp_eq_u32_e64 s[0:1], 0, v202
	v_and_b32_e32 v3, 32, v0
	s_xor_b64 s[26:27], vcc, s[24:25]
	v_writelane_b32 v255, s0, 30
	s_xor_b64 s[28:29], vcc, s[16:17]
	s_xor_b64 s[30:31], vcc, s[10:11]
	v_writelane_b32 v255, s1, 31
	v_cmp_eq_u32_e64 s[0:1], 1, v202
	s_xor_b64 s[34:35], vcc, s[6:7]
	v_cmp_ne_u32_e32 vcc, 0, v3
	v_writelane_b32 v255, s0, 32
	v_cmp_eq_u32_e64 s[36:37], 0, v4
	s_xor_b64 s[38:39], vcc, s[36:37]
	v_writelane_b32 v255, s1, 33
	v_cmp_eq_u32_e64 s[0:1], 2, v202
	s_xor_b64 s[40:41], vcc, s[24:25]
	s_xor_b64 s[42:43], vcc, s[16:17]
	v_writelane_b32 v255, s0, 34
	s_xor_b64 s[44:45], vcc, s[10:11]
	s_xor_b64 s[46:47], vcc, s[6:7]
	v_writelane_b32 v255, s1, 35
	v_cmp_eq_u32_e64 s[0:1], 3, v202
	s_mov_b32 s61, 0
	v_and_b32_e32 v1, 31, v0
	v_writelane_b32 v255, s0, 36
	v_or_b32_e32 v16, 64, v202
	v_lshl_add_u32 v27, v8, 2, 0
	v_writelane_b32 v255, s1, 37
	v_cmp_eq_u32_e64 s[0:1], 4, v202
	v_lshlrev_b32_e32 v32, 2, v5
	v_cmp_eq_u32_e64 s[48:49], 0, v3
	v_writelane_b32 v255, s0, 38
	s_mov_b32 s33, 0x7fffff80
	v_mov_b32_e32 v37, 0x358637bd
	v_writelane_b32 v255, s1, 39
	v_cmp_eq_u32_e64 s[0:1], 5, v202
	v_mov_b32_e32 v38, 0x260
	s_brev_b32 s8, -2
	v_writelane_b32 v255, s0, 40
	s_nop 1
	v_writelane_b32 v255, s1, 41
	v_cmp_eq_u32_e64 s[0:1], 6, v202
	s_nop 1
	v_writelane_b32 v255, s0, 42
	s_nop 1
	v_writelane_b32 v255, s1, 43
	v_cmp_eq_u32_e64 s[0:1], 7, v202
	s_nop 1
	v_writelane_b32 v255, s0, 44
	s_nop 1
	v_writelane_b32 v255, s1, 45
	v_cmp_eq_u32_e64 s[0:1], 8, v202
	s_nop 1
	v_writelane_b32 v255, s0, 46
	s_nop 1
	v_writelane_b32 v255, s1, 47
	s_add_u32 s0, s66, 0x27c00000
	s_addc_u32 s1, s67, 0
	v_writelane_b32 v255, s0, 48
	s_nop 1
	v_writelane_b32 v255, s1, 49
	s_add_u32 s0, s66, 0x27e00000
	s_addc_u32 s1, s67, 0
	v_writelane_b32 v255, s0, 50
	s_nop 1
	v_writelane_b32 v255, s1, 51
	s_lshl_b32 s0, s4, 11
	s_lshl_b32 s1, s4, 2
	s_add_i32 s0, s0, 0
	v_writelane_b32 v255, s0, 52
	v_add_u32_e32 v33, s0, v2
	s_or_b32 s0, s1, 1
	v_writelane_b32 v255, s0, 53
	s_lshl_b32 s0, s0, 9
	s_add_i32 s0, s0, 0
	v_writelane_b32 v255, s0, 54
	v_add_u32_e32 v34, s0, v2
	s_or_b32 s0, s1, 2
	v_writelane_b32 v255, s0, 55
	s_lshl_b32 s0, s0, 9
	s_add_i32 s0, s0, 0
	v_writelane_b32 v255, s0, 56
	v_add_u32_e32 v35, s0, v2
	v_writelane_b32 v255, s1, 57
	s_or_b32 s0, s1, 3
	v_writelane_b32 v255, s0, 58
	s_lshl_b32 s0, s0, 9
	s_add_i32 s0, s0, 0
	v_writelane_b32 v255, s0, 59
	v_add_u32_e32 v36, s0, v2
	s_branch .LBB0_774
